# v58: v56 + back-edge rotation (partial): attention tile-loop bookkeeping hoisted above the loop-back barrier in both loops
# baseline (speedup 1.0000x reference)
.Lmla_dma_v3:
	s_add_i32 s12, s86, 2
	s_min_i32 s12, s12, s78
	s_ashr_i32 s13, s12, 31
	s_add_i32 s15, s80, 0x6000
	s_lshl_b64 s[12:13], s[12:13], 16
	s_and_b32 s15, s15, 0x6000
	v_readlane_b32 s16, v254, 34
	s_add_i32 s15, s15, s16
	v_lshl_add_u64 v[196:197], v[114:115], 0, s[12:13]
	s_mov_b32 s12, m0
	s_mov_b32 m0, s15
	s_nop 0
	global_load_lds_dwordx4 v[196:197], off
	s_mov_b32 m0, s12
	s_add_i32 s4, s81, s83
	s_addk_i32 s80, 0x2000
	s_add_i32 s82, s82, 64
	v_subrev_u32_e32 v122, 64, v122
	s_and_b64 vcc, exec, s[6:7]
	s_cbranch_vccz .LBB0_1056

.LBB0_1053:
	s_cmp_eq_u32 s4, 1
	s_cbranch_scc1 .LBB0_1069
	s_mov_b32 s86, s83
	s_branch .LBB0_1037

.LBB0_1100:
	global_load_dword v175, v1, s[94:95] offset:4
	s_add_i32 s5, s78, 3
	s_min_i32 s5, s5, s81
	v_mad_i64_i32 v[200:201], s[12:13], s5, v235, v[182:183]
	s_add_i32 s5, s89, 0x2000
	s_and_b32 s5, s5, 0x6000
	s_add_i32 s5, s5, s85
	s_mov_b32 s12, m0
	s_mov_b32 m0, s5
	s_nop 0
	global_load_lds_dwordx4 v[200:201], off
	s_mov_b32 m0, s12
	s_add_i32 s5, s78, 2
	s_min_i32 s5, s5, s81
	s_add_i32 s12, s88, 0xc000
	s_and_b32 s15, s12, 0xc000
	v_mad_i64_i32 v[200:201], s[12:13], s5, v235, v[150:151]
	s_add_i32 s12, s15, s75
	s_mov_b32 s13, m0
	s_mov_b32 m0, s12
	s_nop 0
	global_load_lds_dwordx4 v[200:201], off
	s_mov_b32 m0, s13
	v_mad_i64_i32 v[200:201], s[12:13], s5, v235, v[152:153]
	s_add_i32 s5, s15, s74
	s_mov_b32 s12, m0
	s_mov_b32 m0, s5
	s_nop 0
	global_load_lds_dwordx4 v[200:201], off
	s_mov_b32 m0, s12
	s_add_u32 s94, s94, 4
	s_addc_u32 s95, s95, 0
	s_addk_i32 s89, 0x2000
	s_add_i32 s5, s1, s4
	s_addk_i32 s88, 0x4000
	s_add_i32 s93, s93, 64
	v_subrev_u32_e32 v169, 64, v169
	v_add_u32_e32 v167, 0x100, v167
	s_and_b64 vcc, exec, s[6:7]
	s_cbranch_vccz .LBB0_1107

.LBB0_1104:
	s_cmp_eq_u32 s5, 1
	s_cbranch_scc1 .LBB0_1120
	s_mov_b32 s78, s4
	s_branch .LBB0_1088
